# speedup vs baseline: 1.0490x; 1.0105x over previous
.LBB2_102:
	s_or_b64 exec, exec, s[0:1]
	s_lshl_b32 s94, s14, 2
	s_add_i32 s94, s94, s77
	s_add_i32 s94, s94, -1
	s_add_i32 s95, s33, -1
	s_lshl_b32 s96, s86, 12
	v_mov_b32_e32 v250, v0
	v_lshrrev_b32_e32 v251, 5, v250
	v_and_b32_e32 v252, 31, v250
	v_mul_u32_u24_e32 v253, 0xcd, v251
	v_lshrrev_b32_e32 v253, 11, v253
	v_mad_i32_i24 v254, v253, -10, v251
	v_add_u32_e32 v253, s94, v253
	v_add_u32_e32 v254, s95, v254
	v_med3_i32 v253, v253, 0, 63
	v_med3_i32 v254, v254, 0, 63
	v_lshl_add_u32 v253, v253, 6, v254
	v_add_u32_e32 v253, s96, v253
	v_lshlrev_b32_e32 v253, 9, v253
	v_lshl_add_u32 v253, v252, 4, v253
	global_load_dwordx4 v[234:237], v253, s[68:69]
	v_add_u32_e32 v250, 0x200, v0
	v_lshrrev_b32_e32 v251, 5, v250
	v_and_b32_e32 v252, 31, v250
	v_mul_u32_u24_e32 v253, 0xcd, v251
	v_lshrrev_b32_e32 v253, 11, v253
	v_mad_i32_i24 v254, v253, -10, v251
	v_add_u32_e32 v253, s94, v253
	v_add_u32_e32 v254, s95, v254
	v_med3_i32 v253, v253, 0, 63
	v_med3_i32 v254, v254, 0, 63
	v_lshl_add_u32 v253, v253, 6, v254
	v_add_u32_e32 v253, s96, v253
	v_lshlrev_b32_e32 v253, 9, v253
	v_lshl_add_u32 v253, v252, 4, v253
	global_load_dwordx4 v[238:241], v253, s[68:69]
	v_add_u32_e32 v250, 0x400, v0
	v_lshrrev_b32_e32 v251, 5, v250
	v_and_b32_e32 v252, 31, v250
	v_mul_u32_u24_e32 v253, 0xcd, v251
	v_lshrrev_b32_e32 v253, 11, v253
	v_mad_i32_i24 v254, v253, -10, v251
	v_add_u32_e32 v253, s94, v253
	v_add_u32_e32 v254, s95, v254
	v_med3_i32 v253, v253, 0, 63
	v_med3_i32 v254, v254, 0, 63
	v_lshl_add_u32 v253, v253, 6, v254
	v_add_u32_e32 v253, s96, v253
	v_lshlrev_b32_e32 v253, 9, v253
	v_lshl_add_u32 v253, v252, 4, v253
	global_load_dwordx4 v[242:245], v253, s[68:69]
	v_add_u32_e32 v250, 0x600, v0
	v_min_u32_e32 v250, 0x77f, v250
	v_lshrrev_b32_e32 v251, 5, v250
	v_and_b32_e32 v252, 31, v250
	v_mul_u32_u24_e32 v253, 0xcd, v251
	v_lshrrev_b32_e32 v253, 11, v253
	v_mad_i32_i24 v254, v253, -10, v251
	v_add_u32_e32 v253, s94, v253
	v_add_u32_e32 v254, s95, v254
	v_med3_i32 v253, v253, 0, 63
	v_med3_i32 v254, v254, 0, 63
	v_lshl_add_u32 v253, v253, 6, v254
	v_add_u32_e32 v253, s96, v253
	v_lshlrev_b32_e32 v253, 9, v253
	v_lshl_add_u32 v253, v252, 4, v253
	global_load_dwordx4 v[246:249], v253, s[68:69]
	v_lshl_or_b32 v232, s2, 9, v0
	v_lshlrev_b32_e32 v232, 4, v232
	global_load_dwordx4 v[216:219], v232, s[62:63] nt
	v_add_u32_e32 v233, 0x200000, v232
	global_load_dwordx4 v[220:223], v233, s[62:63] nt
	v_add_u32_e32 v233, 0x400000, v232
	global_load_dwordx4 v[224:227], v233, s[62:63] nt
	v_add_u32_e32 v233, 0x600000, v232
	global_load_dwordx4 v[228:231], v233, s[62:63] nt
	v_lshl_add_u32 v42, v46, 1, 0
	s_movk_i32 s3, 0x110
	v_mad_u32_u24 v43, v44, s3, v42
	s_waitcnt vmcnt(17)
	ds_write_b128 v43, v[6:9]
	v_mad_u32_u24 v6, v45, s3, v42
	s_waitcnt vmcnt(16)
	ds_write_b128 v6, v[2:5]
	v_mad_u32_u24 v2, v47, s3, v42
	s_waitcnt vmcnt(15)
	ds_write_b128 v2, v[14:17]
	v_mad_u32_u24 v2, v48, s3, v42
	s_waitcnt vmcnt(14)
	ds_write_b128 v2, v[10:13]
	v_mad_u32_u24 v2, v49, s3, v42
	s_waitcnt vmcnt(13)
	ds_write_b128 v2, v[22:25]
	v_lshrrev_b32_e32 v2, 4, v120
	s_movk_i32 s0, 0xe10
	s_lshl_b64 s[4:5], s[86:87], 19
	v_mad_u32_u24 v2, v2, s3, v42
	v_cmp_gt_u32_e32 vcc, s0, v1
	s_waitcnt vmcnt(12)
	ds_write_b128 v2, v[18:21]
	s_and_saveexec_b64 s[0:1], vcc
	s_cbranch_execz .LBB2_104
	v_lshrrev_b32_e32 v1, 4, v1
	v_mad_u32_u24 v1, v1, s3, v42
	s_waitcnt vmcnt(11)
	ds_write_b128 v1, v[30:33]
.LBB2_104:
	s_or_b64 exec, exec, s[0:1]
	v_cmp_gt_u32_e32 vcc, 16, v0
	s_and_saveexec_b64 s[0:1], vcc
	s_cbranch_execz .LBB2_106
	s_waitcnt vmcnt(10)
	ds_write_b128 v42, v[26:29] offset:60928
.LBB2_106:
	s_or_b64 exec, exec, s[0:1]
	s_movk_i32 s0, 0x3c0
	v_cmp_gt_u32_e32 vcc, s0, v0
	s_and_saveexec_b64 s[0:1], vcc
	s_cbranch_execz .LBB2_108
	v_mul_u32_u24_e32 v1, 0x110, v44
	v_add_u32_e32 v1, v42, v1
	s_waitcnt vmcnt(9)
	ds_write_b128 v1, v[38:41] offset:61200
.LBB2_108:
	s_or_b64 exec, exec, s[0:1]
	s_movk_i32 s0, 0x1c0
	v_cmp_gt_u32_e32 vcc, s0, v0
	s_and_saveexec_b64 s[0:1], vcc
	s_cbranch_execz .LBB2_110
	v_mul_u32_u24_e32 v1, 0x110, v45
	v_add_u32_e32 v1, v42, v1
	s_waitcnt vmcnt(8)
	ds_write_b128 v1, v[34:37] offset:61200
.LBB2_110:
	s_or_b64 exec, exec, s[0:1]
	s_waitcnt vmcnt(4)
	v_mov_b32_e32 v250, v0
	v_lshrrev_b32_e32 v251, 5, v250
	v_and_b32_e32 v252, 31, v250
	v_lshlrev_b32_e32 v251, 9, v251
	v_and_b32_e32 v253, 1, v252
	v_lshrrev_b32_e32 v252, 1, v252
	v_lshl_add_u32 v251, v253, 8, v251
	v_lshl_add_u32 v251, v252, 4, v251
	v_add_u32_e32 v251, 0x13e00, v251
	ds_write_b128 v251, v[234:237]
	v_add_u32_e32 v250, 0x200, v0
	v_lshrrev_b32_e32 v251, 5, v250
	v_and_b32_e32 v252, 31, v250
	v_lshlrev_b32_e32 v251, 9, v251
	v_and_b32_e32 v253, 1, v252
	v_lshrrev_b32_e32 v252, 1, v252
	v_lshl_add_u32 v251, v253, 8, v251
	v_lshl_add_u32 v251, v252, 4, v251
	v_add_u32_e32 v251, 0x13e00, v251
	ds_write_b128 v251, v[238:241]
	v_add_u32_e32 v250, 0x400, v0
	v_lshrrev_b32_e32 v251, 5, v250
	v_and_b32_e32 v252, 31, v250
	v_lshlrev_b32_e32 v251, 9, v251
	v_and_b32_e32 v253, 1, v252
	v_lshrrev_b32_e32 v252, 1, v252
	v_lshl_add_u32 v251, v253, 8, v251
	v_lshl_add_u32 v251, v252, 4, v251
	v_add_u32_e32 v251, 0x13e00, v251
	ds_write_b128 v251, v[242:245]
	v_add_u32_e32 v250, 0x600, v0
	v_lshrrev_b32_e32 v251, 5, v250
	v_and_b32_e32 v252, 31, v250
	v_lshlrev_b32_e32 v251, 9, v251
	v_and_b32_e32 v253, 1, v252
	v_lshrrev_b32_e32 v252, 1, v252
	v_lshl_add_u32 v251, v253, 8, v251
	v_lshl_add_u32 v251, v252, 4, v251
	v_add_u32_e32 v251, 0x13e00, v251
	v_cmp_gt_u32_e32 vcc, 0x180, v0
	s_and_saveexec_b64 s[98:99], vcc
	ds_write_b128 v251, v[246:249]
	s_or_b64 exec, exec, s[98:99]
	v_bfe_u32 v65, v0, 6, 1
	v_bfe_u32 v1, v0, 3, 1
	v_lshl_or_b32 v46, v65, 1, v1
	v_lshrrev_b32_e32 v1, 3, v0
	v_and_b32_e32 v97, 15, v0
	v_and_b32_e32 v1, 48, v1
	v_or_b32_e32 v63, v1, v97
	v_mul_lo_u16_e32 v2, 20, v63
	v_lshrrev_b16_e32 v2, 7, v2
	v_and_b32_e32 v2, 14, v2
	v_or_b32_e32 v110, 64, v63
	v_add_u32_sdwa v6, v63, v2 dst_sel:DWORD dst_unused:UNUSED_PAD src0_sel:DWORD src1_sel:WORD_0
	v_mul_lo_u16_e32 v2, 0x4f, v110
	v_lshrrev_b16_e32 v2, 9, v2
	v_and_b32_e32 v2, 62, v2
	v_bfe_u32 v62, v0, 4, 2
	v_and_b32_e32 v47, 7, v0
	v_add_u32_e32 v10, v110, v2
	v_lshl_add_u32 v84, v62, 4, 0
	v_mad_u32_u24 v2, v46, 10, v47
	s_movk_i32 s0, 0x110
	s_waitcnt vmcnt(4)
	v_mad_u32_u24 v34, v2, s0, v84
	s_waitcnt lgkmcnt(0)
	s_barrier
	ds_read_b128 v[2:5], v34 offset:61200
	v_or_b32_e32 v64, 0x80, v63
	v_min_u32_e32 v22, 0xa8, v64
	v_mul_lo_u16_e32 v7, 0x4f, v22
	v_lshrrev_b32_e32 v180, 4, v1
	v_lshrrev_b32_e32 v181, 1, v180
	v_and_b32_e32 v182, 1, v180
	v_lshl_or_b32 v181, v181, 5, v182
	v_add_u32_e32 v183, 4, v97
	v_add_u32_e32 v184, -8, v97
	v_cmp_gt_u32_e64 s[90:91], 4, v97
	v_cmp_lt_u32_e64 s[92:93], 11, v97
	v_mov_b32_e32 v188, 0xc0
	s_nop 0
	v_cndmask_b32_e64 v183, v183, v97, s[90:91]
	v_cndmask_b32_e64 v183, v183, v184, s[92:93]
	v_lshl_add_u32 v185, v183, 1, v181
	v_add_u32_e32 v186, 64, v185
	v_add_u32_e32 v187, 0x80, v185
	v_cmp_eq_u32_e32 vcc, 0xa4, v187
	s_nop 1
	v_cndmask_b32_e32 v187, v187, v188, vcc
	v_mul_u32_u24_e32 v189, 0x89, v185
	v_lshrrev_b32_e32 v189, 11, v189
	v_mad_i32_i24 v190, v189, -15, v185
	v_cmp_gt_u32_e32 vcc, 13, v190
	v_lshlrev_b32_e32 v191, 1, v189
	v_sub_u32_e32 v193, v185, v191
	v_mad_u32_u24 v98, v185, s0, v84
	v_cndmask_b32_e64 v196, 0, 1, vcc
	v_mul_u32_u24_e32 v189, 0x89, v186
	v_lshrrev_b32_e32 v189, 11, v189
	v_mad_i32_i24 v190, v189, -15, v186
	v_cmp_gt_u32_e32 vcc, 13, v190
	v_lshlrev_b32_e32 v191, 1, v189
	v_sub_u32_e32 v194, v186, v191
	v_mad_u32_u24 v111, v186, s0, v84
	v_cndmask_b32_e64 v197, 0, 1, vcc
	v_mul_u32_u24_e32 v189, 0x89, v187
	v_lshrrev_b32_e32 v189, 11, v189
	v_mad_i32_i24 v190, v189, -15, v187
	v_cmp_gt_u32_e32 vcc, 13, v190
	v_lshlrev_b32_e32 v191, 1, v189
	v_sub_u32_e32 v195, v187, v191
	v_mad_u32_u24 v117, v187, s0, v84
	v_cndmask_b32_e64 v198, 0, 1, vcc
	v_lshrrev_b16_e32 v23, 9, v7
	ds_read_b128 v[6:9], v98
	ds_read_b128 v[10:13], v111
	ds_read_b128 v[14:17], v34 offset:61264
	ds_read_b128 v[18:21], v98 offset:64
	v_and_b32_e32 v23, 30, v23
	s_waitcnt lgkmcnt(3)
	v_mfma_f32_16x16x32_f16 v[6:9], v[2:5], v[6:9], 0
	v_add_u32_e32 v26, v22, v23
	ds_read_b128 v[22:25], v111 offset:64
	ds_read_b128 v[26:29], v117
	ds_read_b128 v[30:33], v117 offset:64
	s_waitcnt lgkmcnt(3)
	v_mfma_f32_16x16x32_f16 v[6:9], v[14:17], v[18:21], v[6:9]
	ds_read_b128 v[18:21], v34 offset:61328
	v_add_u32_e32 v58, 1, v47
	v_add_u32_e32 v85, 2, v47
	v_mfma_f32_16x16x32_f16 v[10:13], v[2:5], v[10:13], 0
	v_lshl_or_b32 v86, s2, 9, v0
	v_ashrrev_i32_e32 v87, 31, v86
	v_lshlrev_b64 v[74:75], 4, v[86:87]
	s_waitcnt lgkmcnt(2)
	v_mfma_f32_16x16x32_f16 v[2:5], v[2:5], v[26:29], 0
	v_mad_u32_u24 v90, v46, 10, 20
	v_lshl_add_u64 v[70:71], s[60:61], 0, v[74:75]
	v_add_co_u32_e32 v42, vcc, 0x200000, v70
	v_mfma_f32_16x16x32_f16 v[10:13], v[14:17], v[22:25], v[10:13]
	s_nop 0
	v_addc_co_u32_e32 v43, vcc, 0, v71, vcc
	v_add_co_u32_e32 v50, vcc, 0x400000, v70
	s_waitcnt lgkmcnt(1)
	v_mfma_f32_16x16x32_f16 v[2:5], v[14:17], v[30:33], v[2:5]
	ds_read_b128 v[14:17], v98 offset:128
	ds_read_b128 v[22:25], v34 offset:61392
	ds_read_b128 v[26:29], v98 offset:192
	v_addc_co_u32_e32 v51, vcc, 0, v71, vcc
	s_waitcnt lgkmcnt(2)
	v_mfma_f32_16x16x32_f16 v[6:9], v[18:21], v[14:17], v[6:9]
	ds_read_b128 v[14:17], v111 offset:128
	ds_read_b128 v[30:33], v111 offset:192
	v_add_co_u32_e32 v52, vcc, 0x600000, v70
	s_waitcnt lgkmcnt(1)
	v_mfma_f32_16x16x32_f16 v[10:13], v[18:21], v[14:17], v[10:13]
	ds_read_b128 v[14:17], v117 offset:128
	ds_read_b128 v[34:37], v117 offset:192
	v_addc_co_u32_e32 v53, vcc, 0, v71, vcc
	s_waitcnt lgkmcnt(1)
	v_mfma_f32_16x16x32_f16 v[2:5], v[18:21], v[14:17], v[2:5]
	v_mad_u32_u24 v14, v46, 10, v58
	v_mad_u32_u24 v38, v14, s0, v84
	ds_read_b128 v[14:17], v38 offset:61200
	v_mfma_f32_16x16x32_f16 v[6:9], v[22:25], v[26:29], v[6:9]
	v_add_co_u32_e32 v54, vcc, 0x800000, v70
	s_mov_b32 s1, 0x200000
	v_mfma_f32_16x16x32_f16 v[10:13], v[22:25], v[30:33], v[10:13]
	v_addc_co_u32_e32 v55, vcc, 0, v71, vcc
	v_lshl_add_u64 v[82:83], s[62:63], 0, v[74:75]
	s_waitcnt lgkmcnt(1)
	v_mfma_f32_16x16x32_f16 v[2:5], v[22:25], v[34:37], v[2:5]
	ds_read_b128 v[18:21], v98 offset:272
	ds_read_b128 v[22:25], v38 offset:61264
	ds_read_b128 v[26:29], v98 offset:336
	s_mov_b32 s2, 0x400000
	s_mov_b32 s3, 0x600000
	s_waitcnt lgkmcnt(2)
	v_mfma_f32_16x16x32_f16 v[6:9], v[14:17], v[18:21], v[6:9]
	ds_read_b128 v[18:21], v111 offset:272
	ds_read_b128 v[30:33], v111 offset:336
	s_add_i32 s6, 0, 0x13890
	s_waitcnt lgkmcnt(1)
	v_mfma_f32_16x16x32_f16 v[10:13], v[14:17], v[18:21], v[10:13]
	ds_read_b128 v[18:21], v117 offset:272
	ds_read_b128 v[34:37], v117 offset:336
	s_waitcnt lgkmcnt(1)
	v_mfma_f32_16x16x32_f16 v[2:5], v[14:17], v[18:21], v[2:5]
	ds_read_b128 v[14:17], v38 offset:61328
	v_mfma_f32_16x16x32_f16 v[6:9], v[22:25], v[26:29], v[6:9]
	v_mfma_f32_16x16x32_f16 v[10:13], v[22:25], v[30:33], v[10:13]
	s_waitcnt lgkmcnt(1)
	v_mfma_f32_16x16x32_f16 v[2:5], v[22:25], v[34:37], v[2:5]
	ds_read_b128 v[18:21], v98 offset:400
	ds_read_b128 v[22:25], v38 offset:61392
	ds_read_b128 v[26:29], v98 offset:464
	s_waitcnt lgkmcnt(2)
	v_mfma_f32_16x16x32_f16 v[6:9], v[14:17], v[18:21], v[6:9]
	ds_read_b128 v[18:21], v111 offset:400
	ds_read_b128 v[30:33], v111 offset:464
	s_waitcnt lgkmcnt(1)
	v_mfma_f32_16x16x32_f16 v[10:13], v[14:17], v[18:21], v[10:13]
	ds_read_b128 v[18:21], v117 offset:400
	ds_read_b128 v[34:37], v117 offset:464
	s_waitcnt lgkmcnt(1)
	v_mfma_f32_16x16x32_f16 v[2:5], v[14:17], v[18:21], v[2:5]
	v_mad_u32_u24 v14, v46, 10, v85
	v_mad_u32_u24 v38, v14, s0, v84
	ds_read_b128 v[14:17], v38 offset:61200
	v_mfma_f32_16x16x32_f16 v[6:9], v[22:25], v[26:29], v[6:9]
	v_mfma_f32_16x16x32_f16 v[10:13], v[22:25], v[30:33], v[10:13]
	s_waitcnt lgkmcnt(1)
	v_mfma_f32_16x16x32_f16 v[2:5], v[22:25], v[34:37], v[2:5]
	ds_read_b128 v[18:21], v98 offset:544
	ds_read_b128 v[22:25], v38 offset:61264
	ds_read_b128 v[26:29], v98 offset:608
	s_waitcnt lgkmcnt(2)
	v_mfma_f32_16x16x32_f16 v[6:9], v[14:17], v[18:21], v[6:9]
	ds_read_b128 v[18:21], v111 offset:544
	ds_read_b128 v[30:33], v111 offset:608
	s_waitcnt lgkmcnt(1)
	v_mfma_f32_16x16x32_f16 v[10:13], v[14:17], v[18:21], v[10:13]
	ds_read_b128 v[18:21], v117 offset:544
	ds_read_b128 v[34:37], v117 offset:608
	s_waitcnt lgkmcnt(1)
	v_mfma_f32_16x16x32_f16 v[2:5], v[14:17], v[18:21], v[2:5]
	ds_read_b128 v[14:17], v38 offset:61328
	v_mfma_f32_16x16x32_f16 v[6:9], v[22:25], v[26:29], v[6:9]
	v_mfma_f32_16x16x32_f16 v[10:13], v[22:25], v[30:33], v[10:13]
	s_waitcnt lgkmcnt(1)
	v_mfma_f32_16x16x32_f16 v[2:5], v[22:25], v[34:37], v[2:5]
	ds_read_b128 v[18:21], v98 offset:672
	ds_read_b128 v[22:25], v38 offset:61392
	ds_read_b128 v[26:29], v98 offset:736
	v_mad_u32_u24 v38, v46, 10, 10
	s_waitcnt lgkmcnt(2)
	v_mfma_f32_16x16x32_f16 v[6:9], v[14:17], v[18:21], v[6:9]
	ds_read_b128 v[18:21], v111 offset:672
	ds_read_b128 v[30:33], v111 offset:736
	s_waitcnt lgkmcnt(1)
	v_mfma_f32_16x16x32_f16 v[10:13], v[14:17], v[18:21], v[10:13]
	ds_read_b128 v[18:21], v117 offset:672
	ds_read_b128 v[34:37], v117 offset:736
	s_waitcnt lgkmcnt(1)
	v_mfma_f32_16x16x32_f16 v[2:5], v[14:17], v[18:21], v[2:5]
	v_add_u32_e32 v14, v47, v38
	v_mad_u32_u24 v39, v14, s0, v84
	ds_read_b128 v[14:17], v39 offset:61200
	v_mfma_f32_16x16x32_f16 v[6:9], v[22:25], v[26:29], v[6:9]
	v_mfma_f32_16x16x32_f16 v[10:13], v[22:25], v[30:33], v[10:13]
	s_waitcnt lgkmcnt(1)
	v_mfma_f32_16x16x32_f16 v[2:5], v[22:25], v[34:37], v[2:5]
	ds_read_b128 v[18:21], v98 offset:4080
	ds_read_b128 v[22:25], v39 offset:61264
	ds_read_b128 v[26:29], v98 offset:4144
	s_waitcnt lgkmcnt(2)
	v_mfma_f32_16x16x32_f16 v[6:9], v[14:17], v[18:21], v[6:9]
	ds_read_b128 v[18:21], v111 offset:4080
	ds_read_b128 v[30:33], v111 offset:4144
	s_waitcnt lgkmcnt(1)
	v_mfma_f32_16x16x32_f16 v[10:13], v[14:17], v[18:21], v[10:13]
	ds_read_b128 v[18:21], v117 offset:4080
	ds_read_b128 v[34:37], v117 offset:4144
	s_waitcnt lgkmcnt(1)
	v_mfma_f32_16x16x32_f16 v[2:5], v[14:17], v[18:21], v[2:5]
	ds_read_b128 v[14:17], v39 offset:61328
	v_mfma_f32_16x16x32_f16 v[6:9], v[22:25], v[26:29], v[6:9]
	v_mfma_f32_16x16x32_f16 v[10:13], v[22:25], v[30:33], v[10:13]
	s_waitcnt lgkmcnt(1)
	v_mfma_f32_16x16x32_f16 v[2:5], v[22:25], v[34:37], v[2:5]
	ds_read_b128 v[18:21], v98 offset:4208
	ds_read_b128 v[22:25], v39 offset:61392
	ds_read_b128 v[26:29], v98 offset:4272
	s_waitcnt lgkmcnt(2)
	v_mfma_f32_16x16x32_f16 v[6:9], v[14:17], v[18:21], v[6:9]
	ds_read_b128 v[18:21], v111 offset:4208
	ds_read_b128 v[30:33], v111 offset:4272
	s_waitcnt lgkmcnt(1)
	v_mfma_f32_16x16x32_f16 v[10:13], v[14:17], v[18:21], v[10:13]
	ds_read_b128 v[18:21], v117 offset:4208
	ds_read_b128 v[34:37], v117 offset:4272
	s_waitcnt lgkmcnt(1)
	v_mfma_f32_16x16x32_f16 v[2:5], v[14:17], v[18:21], v[2:5]
	v_add_u32_e32 v14, v58, v38
	v_mad_u32_u24 v39, v14, s0, v84
	ds_read_b128 v[14:17], v39 offset:61200
	v_mfma_f32_16x16x32_f16 v[6:9], v[22:25], v[26:29], v[6:9]
	v_mfma_f32_16x16x32_f16 v[10:13], v[22:25], v[30:33], v[10:13]
	s_waitcnt lgkmcnt(1)
	v_mfma_f32_16x16x32_f16 v[2:5], v[22:25], v[34:37], v[2:5]
	ds_read_b128 v[18:21], v98 offset:4352
	ds_read_b128 v[22:25], v39 offset:61264
	ds_read_b128 v[26:29], v98 offset:4416
	s_waitcnt lgkmcnt(2)
	v_mfma_f32_16x16x32_f16 v[6:9], v[14:17], v[18:21], v[6:9]
	ds_read_b128 v[18:21], v111 offset:4352
	ds_read_b128 v[30:33], v111 offset:4416
	s_waitcnt lgkmcnt(1)
	v_mfma_f32_16x16x32_f16 v[10:13], v[14:17], v[18:21], v[10:13]
	ds_read_b128 v[18:21], v117 offset:4352
	ds_read_b128 v[34:37], v117 offset:4416
	s_waitcnt lgkmcnt(1)
	v_mfma_f32_16x16x32_f16 v[2:5], v[14:17], v[18:21], v[2:5]
	ds_read_b128 v[14:17], v39 offset:61328
	v_mfma_f32_16x16x32_f16 v[6:9], v[22:25], v[26:29], v[6:9]
	v_mfma_f32_16x16x32_f16 v[10:13], v[22:25], v[30:33], v[10:13]
	s_waitcnt lgkmcnt(1)
	v_mfma_f32_16x16x32_f16 v[2:5], v[22:25], v[34:37], v[2:5]
	ds_read_b128 v[18:21], v98 offset:4480
	ds_read_b128 v[22:25], v39 offset:61392
	ds_read_b128 v[26:29], v98 offset:4544
	s_waitcnt lgkmcnt(2)
	v_mfma_f32_16x16x32_f16 v[6:9], v[14:17], v[18:21], v[6:9]
	ds_read_b128 v[18:21], v111 offset:4480
	ds_read_b128 v[30:33], v111 offset:4544
	s_waitcnt lgkmcnt(1)
	v_mfma_f32_16x16x32_f16 v[10:13], v[14:17], v[18:21], v[10:13]
	ds_read_b128 v[18:21], v117 offset:4480
	ds_read_b128 v[34:37], v117 offset:4544
	s_waitcnt lgkmcnt(1)
	v_mfma_f32_16x16x32_f16 v[2:5], v[14:17], v[18:21], v[2:5]
	v_add_u32_e32 v14, v85, v38
	v_mad_u32_u24 v38, v14, s0, v84
	ds_read_b128 v[14:17], v38 offset:61200
	v_mfma_f32_16x16x32_f16 v[6:9], v[22:25], v[26:29], v[6:9]
	v_mfma_f32_16x16x32_f16 v[10:13], v[22:25], v[30:33], v[10:13]
	s_waitcnt lgkmcnt(1)
	v_mfma_f32_16x16x32_f16 v[2:5], v[22:25], v[34:37], v[2:5]
	ds_read_b128 v[18:21], v98 offset:4624
	ds_read_b128 v[22:25], v38 offset:61264
	ds_read_b128 v[26:29], v98 offset:4688
	s_waitcnt lgkmcnt(2)
	v_mfma_f32_16x16x32_f16 v[6:9], v[14:17], v[18:21], v[6:9]
	ds_read_b128 v[18:21], v111 offset:4624
	ds_read_b128 v[30:33], v111 offset:4688
	s_waitcnt lgkmcnt(1)
	v_mfma_f32_16x16x32_f16 v[10:13], v[14:17], v[18:21], v[10:13]
	ds_read_b128 v[18:21], v117 offset:4624
	ds_read_b128 v[34:37], v117 offset:4688
	s_waitcnt lgkmcnt(1)
	v_mfma_f32_16x16x32_f16 v[2:5], v[14:17], v[18:21], v[2:5]
	ds_read_b128 v[14:17], v38 offset:61328
	ds_read_b128 v[18:21], v98 offset:4752
	v_mfma_f32_16x16x32_f16 v[6:9], v[22:25], v[26:29], v[6:9]
	v_mfma_f32_16x16x32_f16 v[10:13], v[22:25], v[30:33], v[10:13]
	s_waitcnt lgkmcnt(2)
	v_mfma_f32_16x16x32_f16 v[22:25], v[22:25], v[34:37], v[2:5]
	s_nop 2
	ds_read_b128 v[2:5], v111 offset:4752
	ds_read_b128 v[26:29], v38 offset:61392
	ds_read_b128 v[30:33], v98 offset:4816
	ds_read_b128 v[34:37], v117 offset:4752
	ds_read_b128 v[38:41], v111 offset:4816
	s_waitcnt lgkmcnt(5)
	v_mfma_f32_16x16x32_f16 v[18:21], v[14:17], v[18:21], v[6:9]
	s_waitcnt lgkmcnt(4)
	v_mfma_f32_16x16x32_f16 v[10:13], v[14:17], v[2:5], v[10:13]
	s_nop 0
	global_load_dwordx4 v[6:9], v[70:71], off nt
	global_load_dwordx4 v[2:5], v[42:43], off nt
	ds_read_b128 v[42:45], v117 offset:4816
	s_waitcnt lgkmcnt(2)
	v_mfma_f32_16x16x32_f16 v[14:17], v[14:17], v[34:37], v[22:25]
	s_nop 2
	v_add_u32_e32 v22, v47, v90
	v_mad_u32_u24 v56, v22, s0, v84
	ds_read_b128 v[22:25], v56 offset:61200
	v_mfma_f32_16x16x32_f16 v[18:21], v[26:29], v[30:33], v[18:21]
	ds_read_b128 v[30:33], v98 offset:8160
	s_waitcnt lgkmcnt(3)
	v_mfma_f32_16x16x32_f16 v[10:13], v[26:29], v[38:41], v[10:13]
	s_waitcnt lgkmcnt(2)
	v_mfma_f32_16x16x32_f16 v[14:17], v[26:29], v[42:45], v[14:17]
	ds_read_b128 v[26:29], v111 offset:8160
	ds_read_b128 v[34:37], v56 offset:61264
	ds_read_b128 v[38:41], v98 offset:8224
	s_waitcnt lgkmcnt(3)
	v_mfma_f32_16x16x32_f16 v[18:21], v[22:25], v[30:33], v[18:21]
	ds_read_b128 v[30:33], v117 offset:8160
	ds_read_b128 v[42:45], v111 offset:8224
	ds_read_b128 v[46:49], v117 offset:8224
	s_waitcnt lgkmcnt(5)
	v_mfma_f32_16x16x32_f16 v[26:29], v[22:25], v[26:29], v[10:13]
	s_waitcnt lgkmcnt(2)
	v_mfma_f32_16x16x32_f16 v[22:25], v[22:25], v[30:33], v[14:17]
	s_nop 2
	global_load_dwordx4 v[14:17], v[50:51], off nt
	global_load_dwordx4 v[10:13], v[52:53], off nt
	ds_read_b128 v[30:33], v56 offset:61328
	v_mfma_f32_16x16x32_f16 v[18:21], v[34:37], v[38:41], v[18:21]
	ds_read_b128 v[38:41], v98 offset:8288
	s_waitcnt lgkmcnt(3)
	v_mfma_f32_16x16x32_f16 v[26:29], v[34:37], v[42:45], v[26:29]
	s_waitcnt lgkmcnt(2)
	v_mfma_f32_16x16x32_f16 v[22:25], v[34:37], v[46:49], v[22:25]
	ds_read_b128 v[34:37], v111 offset:8288
	ds_read_b128 v[42:45], v56 offset:61392
	ds_read_b128 v[46:49], v98 offset:8352
	v_add_co_u32_e32 v56, vcc, 0xa00000, v70
	s_waitcnt lgkmcnt(3)
	v_mfma_f32_16x16x32_f16 v[38:41], v[30:33], v[38:41], v[18:21]
	s_nop 2
	ds_read_b128 v[18:21], v117 offset:8288
	ds_read_b128 v[50:53], v111 offset:8352
	v_addc_co_u32_e32 v57, vcc, 0, v71, vcc
	s_waitcnt lgkmcnt(2)
	v_mfma_f32_16x16x32_f16 v[38:41], v[42:45], v[46:49], v[38:41]
	v_add_u32_e32 v46, v58, v90
	v_mad_u32_u24 v80, v46, s0, v84
	v_add_co_u32_e32 v76, vcc, 0xc00000, v70
	v_mfma_f32_16x16x32_f16 v[26:29], v[30:33], v[34:37], v[26:29]
	ds_read_b128 v[34:37], v117 offset:8352
	v_addc_co_u32_e32 v77, vcc, 0, v71, vcc
	s_waitcnt lgkmcnt(2)
	v_mfma_f32_16x16x32_f16 v[30:33], v[30:33], v[18:21], v[22:25]
	s_nop 2
	global_load_dwordx4 v[22:25], v[54:55], off nt
	global_load_dwordx4 v[18:21], v[56:57], off nt
	ds_read_b128 v[46:49], v80 offset:61200
	v_add_co_u32_e32 v78, vcc, 0xe00000, v70
	s_waitcnt lgkmcnt(2)
	v_mfma_f32_16x16x32_f16 v[26:29], v[42:45], v[50:53], v[26:29]
	ds_read_b128 v[50:53], v98 offset:8432
	v_addc_co_u32_e32 v79, vcc, 0, v71, vcc
	s_waitcnt lgkmcnt(2)
	v_mfma_f32_16x16x32_f16 v[30:33], v[42:45], v[34:37], v[30:33]
	ds_read_b128 v[34:37], v111 offset:8432
	ds_read_b128 v[42:45], v80 offset:61264
	ds_read_b128 v[54:57], v98 offset:8496
	v_add_co_u32_e32 v74, vcc, s1, v82
	s_waitcnt lgkmcnt(3)
	v_mfma_f32_16x16x32_f16 v[38:41], v[46:49], v[50:53], v[38:41]
	ds_read_b128 v[50:53], v117 offset:8432
	ds_read_b128 v[58:61], v111 offset:8496
	ds_read_b128 v[70:73], v117 offset:8496
	v_addc_co_u32_e32 v75, vcc, 0, v83, vcc
	s_waitcnt lgkmcnt(5)
	v_mfma_f32_16x16x32_f16 v[66:69], v[46:49], v[34:37], v[26:29]
	global_load_dwordx4 v[34:37], v[76:77], off nt
	s_nop 1
	global_load_dwordx4 v[26:29], v[78:79], off nt
	v_add_co_u32_e32 v88, vcc, s2, v82
	s_waitcnt lgkmcnt(2)
	v_mfma_f32_16x16x32_f16 v[30:33], v[46:49], v[50:53], v[30:33]
	ds_read_b128 v[46:49], v80 offset:61328
	v_addc_co_u32_e32 v89, vcc, 0, v83, vcc
	v_mfma_f32_16x16x32_f16 v[38:41], v[42:45], v[54:57], v[38:41]
	ds_read_b128 v[54:57], v98 offset:8560
	s_movk_i32 s2, 0xa9
	s_waitcnt lgkmcnt(3)
	v_mfma_f32_16x16x32_f16 v[50:53], v[42:45], v[58:61], v[66:69]
	s_waitcnt lgkmcnt(2)
	v_mfma_f32_16x16x32_f16 v[42:45], v[42:45], v[70:73], v[30:33]
	ds_read_b128 v[58:61], v111 offset:8560
	ds_read_b128 v[66:69], v80 offset:61392
	ds_read_b128 v[70:73], v98 offset:8624
	s_waitcnt lgkmcnt(3)
	v_mfma_f32_16x16x32_f16 v[54:57], v[46:49], v[54:57], v[38:41]
	s_nop 2
	ds_read_b128 v[74:77], v117 offset:8560
	ds_read_b128 v[78:81], v111 offset:8624
	s_waitcnt lgkmcnt(4)
	v_mfma_f32_16x16x32_f16 v[50:53], v[46:49], v[58:61], v[50:53]
	ds_read_b128 v[58:61], v117 offset:8624
	s_waitcnt lgkmcnt(2)
	v_mfma_f32_16x16x32_f16 v[42:45], v[46:49], v[74:77], v[42:45]
	v_mfma_f32_16x16x32_f16 v[46:49], v[66:69], v[70:73], v[54:57]
	ds_read_b128 v[70:73], v98 offset:8704
	s_nop 1
	v_add_u32_e32 v54, v85, v90
	v_mad_u32_u24 v92, v54, s0, v84
	ds_read_b128 v[54:57], v92 offset:61200
	s_waitcnt lgkmcnt(3)
	v_mfma_f32_16x16x32_f16 v[50:53], v[66:69], v[78:81], v[50:53]
	v_add_co_u32_e32 v90, vcc, s3, v82
	s_add_i32 s0, 0, 0x13550
	s_waitcnt lgkmcnt(2)
	v_mfma_f32_16x16x32_f16 v[58:61], v[66:69], v[58:61], v[42:45]
	s_nop 2
	ds_read_b128 v[42:45], v111 offset:8704
	ds_read_b128 v[66:69], v92 offset:61264
	ds_read_b128 v[74:77], v98 offset:8768
	v_addc_co_u32_e32 v91, vcc, 0, v83, vcc
	s_waitcnt lgkmcnt(3)
	v_mfma_f32_16x16x32_f16 v[70:73], v[54:57], v[70:73], v[46:49]
	ds_read_b128 v[78:81], v117 offset:8704
	ds_read_b128 v[82:85], v111 offset:8768
	v_cmp_gt_u32_e64 s[2:3], s2, v64
	v_cmp_eq_u32_e32 vcc, 0, v97
	s_waitcnt lgkmcnt(4)
	v_mfma_f32_16x16x32_f16 v[50:53], v[54:57], v[42:45], v[50:53]
	ds_read_b128 v[88:91], v117 offset:8768
	s_waitcnt lgkmcnt(2)
	v_mfma_f32_16x16x32_f16 v[54:57], v[54:57], v[78:81], v[58:61]
	s_nop 2
	ds_read_b128 v[58:61], v92 offset:61328
	ds_read_b128 v[92:95], v92 offset:61392
	ds_read_b128 v[78:81], v98 offset:8832
	ds_read_b128 v[98:101], v98 offset:8896
	ds_read_b128 v[106:109], v111 offset:8832
	ds_read_b128 v[118:121], v111 offset:8896
	ds_read_b128 v[122:125], v117 offset:8832
	ds_read_b128 v[126:129], v117 offset:8896
	v_mfma_f32_16x16x32_f16 v[102:105], v[66:69], v[74:77], v[70:73]
	s_waitcnt lgkmcnt(9)
	v_mfma_f32_16x16x32_f16 v[50:53], v[66:69], v[82:85], v[50:53]
	s_nop 0
	v_lshlrev_b32_e32 v70, 2, v62
	v_lshl_or_b32 v73, v65, 4, v70
	v_lshl_add_u32 v75, v73, 2, 0
	s_waitcnt lgkmcnt(8)
	v_mfma_f32_16x16x32_f16 v[66:69], v[66:69], v[88:91], v[54:57]
	v_add_u32_e32 v65, 0x13810, v75
	v_min_u32_e32 v72, 0xaf, v64
	v_lshl_add_u32 v70, v63, 2, s0
	s_waitcnt lgkmcnt(5)
	v_mfma_f32_16x16x32_f16 v[54:57], v[58:61], v[78:81], v[102:105]
	v_lshl_add_u32 v71, v110, 2, s0
	v_lshl_add_u32 v72, v72, 2, s0
	ds_read_b32 v65, v65
	ds_read_b32 v79, v70
	ds_read_b32 v78, v71
	ds_read_b32 v77, v72
	s_waitcnt lgkmcnt(7)
	v_mfma_f32_16x16x32_f16 v[80:83], v[58:61], v[106:109], v[50:53]
	s_movk_i32 s0, 0x69
	v_cmp_gt_u32_e64 s[0:1], s0, v63
	s_waitcnt lgkmcnt(5)
	v_mfma_f32_16x16x32_f16 v[58:61], v[58:61], v[122:125], v[66:69]
	v_mfma_f32_16x16x32_f16 v[50:53], v[92:95], v[98:101], v[54:57]
	v_mfma_f32_16x16x32_f16 v[54:57], v[92:95], v[118:121], v[80:83]
	s_waitcnt lgkmcnt(4)
	v_mfma_f32_16x16x32_f16 v[58:61], v[92:95], v[126:129], v[58:61]
	s_waitcnt lgkmcnt(2)
	s_nop 3
	v_or_b32_e32 v69, 1, v73
	v_or_b32_e32 v64, 2, v73
	v_or_b32_e32 v152, 3, v73
	v_lshl_add_u32 v71, v69, 2, 0
	v_lshl_add_u32 v66, v64, 2, 0
	v_lshl_add_u32 v153, v152, 2, 0
	v_add_u32_e32 v160, 0x13810, v71
	v_add_u32_e32 v161, 0x13810, v66
	v_add_u32_e32 v162, 0x13810, v153
	v_mov_b32_e32 v156, 0x13550
	v_lshl_add_u32 v157, v193, 2, v156
	v_lshl_add_u32 v158, v194, 2, v156
	v_lshl_add_u32 v159, v195, 2, v156
	ds_read_b32 v79, v157
	ds_read_b32 v78, v158
	ds_read_b32 v77, v159
	ds_read_b32 v160, v160
	ds_read_b32 v161, v161
	ds_read_b32 v162, v162
	v_mov_b32_e32 v155, 0xff800000
	s_waitcnt lgkmcnt(3)
	v_mul_f32_e32 v164, v50, v79
	v_mul_f32_e32 v165, v54, v78
	v_mul_f32_e32 v166, v58, v77
	v_mul_f32_e32 v164, v65, v164
	v_mul_f32_e32 v165, v65, v165
	v_mul_f32_e32 v166, v65, v166
	v_mul_f32_e32 v167, v51, v79
	v_mul_f32_e32 v168, v55, v78
	v_mul_f32_e32 v169, v59, v77
	v_mul_f32_e32 v170, v52, v79
	v_mul_f32_e32 v171, v56, v78
	v_mul_f32_e32 v172, v60, v77
	v_mul_f32_e32 v173, v53, v79
	v_mul_f32_e32 v174, v57, v78
	v_mul_f32_e32 v175, v61, v77
	s_waitcnt lgkmcnt(0)
	v_mul_f32_e32 v167, v160, v167
	v_mul_f32_e32 v168, v160, v168
	v_mul_f32_e32 v169, v160, v169
	v_mul_f32_e32 v170, v161, v170
	v_mul_f32_e32 v171, v161, v171
	v_mul_f32_e32 v172, v161, v172
	v_mul_f32_e32 v173, v162, v173
	v_mul_f32_e32 v174, v162, v174
	v_mul_f32_e32 v175, v162, v175
	v_cmp_ne_u32_e64 s[8:9], 0, v196
	v_cmp_ne_u32_e64 s[0:1], 0, v197
	v_cmp_ne_u32_e64 s[2:3], 0, v198
	v_cndmask_b32_e64 v164, v155, v164, s[8:9]
	v_cndmask_b32_e64 v167, v155, v167, s[8:9]
	v_cndmask_b32_e64 v170, v155, v170, s[8:9]
	v_cndmask_b32_e64 v173, v155, v173, s[8:9]
	v_cndmask_b32_e64 v165, v155, v165, s[0:1]
	v_cndmask_b32_e64 v166, v155, v166, s[2:3]
	v_cndmask_b32_e64 v168, v155, v168, s[0:1]
	v_cndmask_b32_e64 v169, v155, v169, s[2:3]
	v_cndmask_b32_e64 v171, v155, v171, s[0:1]
	v_cndmask_b32_e64 v172, v155, v172, s[2:3]
	v_cndmask_b32_e64 v174, v155, v174, s[0:1]
	v_cndmask_b32_e64 v175, v155, v175, s[2:3]
	v_max_f32_e32 v176, 0xff800000, v164
	v_max_f32_e32 v177, 0xff800000, v167
	v_max_f32_e32 v178, 0xff800000, v170
	v_max_f32_e32 v179, 0xff800000, v173
	v_max3_f32 v176, v176, v165, v166
	v_max3_f32 v177, v177, v168, v169
	v_max3_f32 v178, v178, v171, v172
	v_max3_f32 v179, v179, v174, v175
	v_max_f32_dpp v176, v176, v176 quad_perm:[1,0,3,2] row_mask:0xf bank_mask:0xf
	v_max_f32_dpp v177, v177, v177 quad_perm:[1,0,3,2] row_mask:0xf bank_mask:0xf
	v_max_f32_dpp v178, v178, v178 quad_perm:[1,0,3,2] row_mask:0xf bank_mask:0xf
	v_max_f32_dpp v179, v179, v179 quad_perm:[1,0,3,2] row_mask:0xf bank_mask:0xf
	v_max_f32_dpp v176, v176, v176 quad_perm:[2,3,0,1] row_mask:0xf bank_mask:0xf
	v_max_f32_dpp v177, v177, v177 quad_perm:[2,3,0,1] row_mask:0xf bank_mask:0xf
	v_max_f32_dpp v178, v178, v178 quad_perm:[2,3,0,1] row_mask:0xf bank_mask:0xf
	v_max_f32_dpp v179, v179, v179 quad_perm:[2,3,0,1] row_mask:0xf bank_mask:0xf
	v_max_f32_dpp v176, v176, v176 row_half_mirror row_mask:0xf bank_mask:0xf
	v_max_f32_dpp v177, v177, v177 row_half_mirror row_mask:0xf bank_mask:0xf
	v_max_f32_dpp v178, v178, v178 row_half_mirror row_mask:0xf bank_mask:0xf
	v_max_f32_dpp v179, v179, v179 row_half_mirror row_mask:0xf bank_mask:0xf
	v_max_f32_dpp v176, v176, v176 row_mirror row_mask:0xf bank_mask:0xf
	v_max_f32_dpp v177, v177, v177 row_mirror row_mask:0xf bank_mask:0xf
	v_max_f32_dpp v178, v178, v178 row_mirror row_mask:0xf bank_mask:0xf
	v_max_f32_dpp v179, v179, v179 row_mirror row_mask:0xf bank_mask:0xf
	v_and_b32_e32 v58, 0x180, v0
	v_add_u32_e32 v58, s6, v58
	v_lshl_add_u32 v58, v73, 2, v58
	s_and_saveexec_b64 s[6:7], vcc
	ds_write_b128 v58, v[176:179]
	s_or_b64 exec, exec, s[6:7]
	v_mov_b32_e32 v76, v164
	v_mov_b32_e32 v74, v165
	v_mov_b32_e32 v72, v166
	v_mov_b32_e32 v70, v167
	v_mov_b32_e32 v68, v168
	v_mov_b32_e32 v67, v169
	v_mov_b32_e32 v65, v170
	v_mov_b32_e32 v59, v171
	v_mov_b32_e32 v56, v172
	v_mov_b32_e32 v53, v173
	v_mov_b32_e32 v52, v174
	v_mov_b32_e32 v50, v175
	v_mov_b32_e32 v54, v152
	v_mov_b32_e32 v55, v153
	v_add_u32_e32 v51, 0x13890, v75
	s_waitcnt lgkmcnt(0)
	s_barrier
	v_add_u32_e32 v152, 0x13890, v75
	ds_read_b128 v[156:159], v152
	ds_read_b128 v[160:163], v152 offset:128
	ds_read_b128 v[164:167], v152 offset:256
	ds_read_b128 v[168:171], v152 offset:384
	v_lshlrev_b32_e32 v51, 3, v62
	v_lshlrev_b32_e32 v60, 8, v73
	v_or_b32_e32 v172, v63, v60
	s_waitcnt lgkmcnt(0)
	v_max_f32_e32 v173, v156, v160
	v_max_f32_e32 v174, v157, v161
	v_max_f32_e32 v175, v158, v162
	v_max_f32_e32 v176, v159, v163
	v_max3_f32 v173, v173, v164, v168
	v_max3_f32 v174, v174, v165, v169
	v_max3_f32 v175, v175, v166, v170
	v_max3_f32 v176, v176, v167, v171
	v_add_f32_e32 v173, 0xbb102de0, v173
	v_add_f32_e32 v174, 0xbb102de0, v174
	v_add_f32_e32 v175, 0xbb102de0, v175
	v_add_f32_e32 v176, 0xbb102de0, v176
	v_cmp_ge_f32_e64 s[90:91], v76, v173
	v_cmp_ge_f32_e64 s[92:93], v74, v173
	v_cmp_ge_f32_e64 s[94:95], v72, v173
	v_cmp_ge_f32_e64 s[96:97], v70, v174
	v_cmp_ge_f32_e64 s[98:99], v68, v174
	v_cmp_ge_f32_e64 s[60:61], v67, v174
	v_cmp_ge_f32_e64 s[62:63], v65, v175
	v_cmp_ge_f32_e64 s[88:89], v59, v175
	v_cmp_ge_f32_e64 s[6:7], v56, v175
	v_cmp_ge_f32_e64 s[8:9], v53, v176
	v_cmp_ge_f32_e64 s[2:3], v52, v176
	v_cmp_ge_f32_e64 s[80:81], v50, v176
	s_bcnt1_i32_b64 s13, s[90:91]
	s_bcnt1_i32_b64 s1, s[92:93]
	s_add_u32 s13, s13, s1
	s_bcnt1_i32_b64 s1, s[94:95]
	s_add_u32 s13, s13, s1
	s_bcnt1_i32_b64 s1, s[96:97]
	s_add_u32 s13, s13, s1
	s_bcnt1_i32_b64 s1, s[98:99]
	s_add_u32 s13, s13, s1
	s_bcnt1_i32_b64 s1, s[60:61]
	s_add_u32 s13, s13, s1
	s_bcnt1_i32_b64 s1, s[62:63]
	s_add_u32 s13, s13, s1
	s_bcnt1_i32_b64 s1, s[88:89]
	s_add_u32 s13, s13, s1
	s_bcnt1_i32_b64 s1, s[6:7]
	s_add_u32 s13, s13, s1
	s_bcnt1_i32_b64 s1, s[8:9]
	s_add_u32 s13, s13, s1
	s_bcnt1_i32_b64 s1, s[2:3]
	s_add_u32 s13, s13, s1
	s_bcnt1_i32_b64 s1, s[80:81]
	s_add_u32 s13, s13, s1
	s_cmp_eq_u32 s13, 0
	s_cbranch_scc1 .Lmy_list_done
	v_mov_b32_e32 v177, 0x13d90
	v_mov_b32_e32 v178, s13
	s_mov_b64 exec, 1
	ds_add_rtn_u32 v179, v177, v178
	s_mov_b64 exec, -1
	s_waitcnt lgkmcnt(0)
	v_readfirstlane_b32 s0, v179
	s_and_saveexec_b64 s[82:83], s[90:91]
	s_cbranch_execz .Lmy_list_skip0
	v_mbcnt_lo_u32_b32 v180, s90, 0
	v_mbcnt_hi_u32_b32 v180, s91, v180
	v_add_u32_e32 v181, 0x0, v60
	v_or_b32_e32 v181, v181, v193
	v_add_lshl_u32 v180, v180, s0, 1
	ds_write_b16 v180, v181
	s_bcnt1_i32_b64 s1, s[90:91]
	s_add_u32 s0, s0, s1

.LBB2_169:
	ds_read_u16 v0, v102
	s_waitcnt lgkmcnt(0)
	v_and_b32_e32 v105, 0xffff, v0
	v_lshrrev_b32_e32 v250, 11, v105
	v_bfe_u32 v251, v105, 8, 3
	v_mad_u32_u24 v250, v250, 10, v251
	v_lshlrev_b32_e32 v250, 9, v250
	v_lshl_add_u32 v250, v97, 4, v250
	v_add_u32_e32 v250, 0x13e00, v250
	v_mul_lo_u16_sdwa v0, v0, s6 dst_sel:DWORD dst_unused:UNUSED_PAD src0_sel:BYTE_0 src1_sel:DWORD
	v_lshrrev_b32_e32 v50, 11, v105
	v_bfe_u32 v54, v105, 8, 3
	v_lshrrev_b16_e32 v52, 10, v0
	v_and_b32_e32 v104, 0xff, v105
	v_add_u32_e32 v55, s12, v54
	v_mul_i32_i24_e32 v0, -13, v52
	v_add_u32_e32 v56, s11, v50
	v_add3_u32 v57, v104, v96, v0
	v_med3_i32 v0, v56, 0, 63
	v_med3_i32 v50, v55, 0, 63
	v_add_lshl_u32 v60, s10, v52, 6
	v_lshlrev_b32_e32 v58, 15, v0
	v_lshlrev_b32_e32 v59, 9, v50
	v_add_u32_e32 v52, v57, v60
	v_or_b32_e32 v0, v58, v59
	v_ashrrev_i32_e32 v53, 31, v52
	v_lshl_add_u64 v[50:51], v[88:89], 0, v[0:1]
	v_lshlrev_b64 v[52:53], 9, v[52:53]
	v_lshl_add_u64 v[52:53], v[90:91], 0, v[52:53]
	ds_read_b128 v[106:109], v250 offset:256
	ds_read_b128 v[70:73], v250
	global_load_dwordx4 v[116:119], v[52:53], off offset:16
	global_load_dwordx4 v[120:123], v[52:53], off
	v_or_b32_e32 v0, s33, v54
	v_add_u32_e32 v61, 1, v57
	v_lshlrev_b32_e32 v54, 9, v0
	v_add_u32_e32 v52, v61, v60
	v_or_b32_e32 v0, v58, v54
	v_ashrrev_i32_e32 v53, 31, v52
	v_lshl_add_u64 v[50:51], v[88:89], 0, v[0:1]
	v_lshlrev_b64 v[52:53], 9, v[52:53]
	v_lshl_add_u64 v[52:53], v[90:91], 0, v[52:53]
	ds_read_b128 v[124:127], v250 offset:768
	ds_read_b128 v[128:131], v250 offset:512
	global_load_dwordx4 v[132:135], v[52:53], off offset:16
	global_load_dwordx4 v[136:139], v[52:53], off
	v_max_i32_e32 v0, -2, v55
	v_add_u32_e32 v0, 2, v0
	v_min_u32_e32 v0, 63, v0
	v_add_u32_e32 v64, 2, v57
	v_lshlrev_b32_e32 v62, 9, v0
	v_add_u32_e32 v52, v64, v60
	v_or_b32_e32 v0, v58, v62
	v_ashrrev_i32_e32 v53, 31, v52
	v_lshl_add_u64 v[50:51], v[88:89], 0, v[0:1]
	v_lshlrev_b64 v[52:53], 9, v[52:53]
	v_lshl_add_u64 v[52:53], v[90:91], 0, v[52:53]
	ds_read_b128 v[140:143], v250 offset:1280
	ds_read_b128 v[144:147], v250 offset:1024
	global_load_dwordx4 v[148:151], v[52:53], off offset:16
	global_load_dwordx4 v[152:155], v[52:53], off
	v_max_i32_e32 v0, -1, v56
	v_add_u32_e32 v0, 1, v0
	v_min_u32_e32 v0, 63, v0
	v_add_u32_e32 v58, 64, v60
	v_lshlrev_b32_e32 v55, 15, v0
	v_add_u32_e32 v52, v57, v58
	v_or_b32_e32 v0, v55, v59
	v_ashrrev_i32_e32 v53, 31, v52
	v_lshl_add_u64 v[50:51], v[88:89], 0, v[0:1]
	v_lshlrev_b64 v[52:53], 9, v[52:53]
	v_lshl_add_u64 v[52:53], v[90:91], 0, v[52:53]
	ds_read_b128 v[156:159], v250 offset:5376
	ds_read_b128 v[160:163], v250 offset:5120
	global_load_dwordx4 v[164:167], v[52:53], off offset:16
	global_load_dwordx4 v[168:171], v[52:53], off
	v_add_u32_e32 v52, v61, v58
	v_or_b32_e32 v0, v55, v54
	v_ashrrev_i32_e32 v53, 31, v52
	v_lshl_add_u64 v[50:51], v[88:89], 0, v[0:1]
	v_lshlrev_b64 v[52:53], 9, v[52:53]
	v_lshl_add_u64 v[52:53], v[90:91], 0, v[52:53]
	ds_read_b128 v[172:175], v250 offset:5888
	ds_read_b128 v[176:179], v250 offset:5632
	global_load_dwordx4 v[180:183], v[52:53], off offset:16
	global_load_dwordx4 v[184:187], v[52:53], off
	v_add_u32_e32 v52, v64, v58
	v_or_b32_e32 v0, v55, v62
	v_ashrrev_i32_e32 v53, 31, v52
	v_lshl_add_u64 v[50:51], v[88:89], 0, v[0:1]
	v_lshlrev_b64 v[52:53], 9, v[52:53]
	v_lshl_add_u64 v[52:53], v[90:91], 0, v[52:53]
	ds_read_b128 v[188:191], v250 offset:6400
	ds_read_b128 v[192:195], v250 offset:6144
	global_load_dwordx4 v[196:199], v[52:53], off offset:16
	global_load_dwordx4 v[200:203], v[52:53], off
	v_max_i32_e32 v0, -2, v56
	v_add_u32_e32 v0, 2, v0
	v_min_u32_e32 v0, 63, v0
	v_add_u32_e32 v65, 0x80, v60
	v_lshlrev_b32_e32 v63, 15, v0
	v_add_u32_e32 v52, v57, v65
	v_or_b32_e32 v0, v63, v59
	v_ashrrev_i32_e32 v53, 31, v52
	v_lshl_add_u64 v[50:51], v[88:89], 0, v[0:1]
	v_lshlrev_b64 v[52:53], 9, v[52:53]
	v_lshl_add_u64 v[52:53], v[90:91], 0, v[52:53]
	ds_read_b128 v[74:77], v250 offset:10496
	ds_read_b128 v[204:207], v250 offset:10240
	global_load_dwordx4 v[82:85], v[52:53], off offset:16
	global_load_dwordx4 v[208:211], v[52:53], off
	v_add_u32_e32 v52, v61, v65
	v_or_b32_e32 v0, v63, v54
	v_ashrrev_i32_e32 v53, 31, v52
	v_lshl_add_u64 v[50:51], v[88:89], 0, v[0:1]
	v_lshlrev_b64 v[52:53], 9, v[52:53]
	v_lshl_add_u64 v[52:53], v[90:91], 0, v[52:53]
	ds_read_b128 v[54:57], v250 offset:11008
	ds_read_b128 v[66:69], v250 offset:10752
	global_load_dwordx4 v[58:61], v[52:53], off offset:16
	global_load_dwordx4 v[78:81], v[52:53], off
	v_add_u32_e32 v50, v64, v65
	v_ashrrev_i32_e32 v51, 31, v50
	v_lshlrev_b64 v[50:51], 9, v[50:51]
	v_lshl_add_u64 v[110:111], v[90:91], 0, v[50:51]
	v_or_b32_e32 v0, v63, v62
	v_lshl_add_u64 v[62:63], v[88:89], 0, v[0:1]
	s_waitcnt lgkmcnt(14)
	v_cvt_f64_f32_e32 v[50:51], v70
	s_waitcnt vmcnt(14)
	v_cvt_f64_f32_e32 v[52:53], v120
	v_fma_f64 v[92:93], v[50:51], v[52:53], 0
	v_cvt_f64_f32_e32 v[50:51], v72
	v_cvt_f64_f32_e32 v[52:53], v122
	v_fmac_f64_e32 v[92:93], v[50:51], v[52:53]
	v_cvt_f64_f32_e32 v[50:51], v71
	v_cvt_f64_f32_e32 v[52:53], v121
	v_fma_f64 v[94:95], v[50:51], v[52:53], 0
	v_cvt_f64_f32_e32 v[70:71], v73
	v_cvt_f64_f32_e32 v[72:73], v123
	v_fmac_f64_e32 v[94:95], v[70:71], v[72:73]
	v_cvt_f64_f32_e32 v[70:71], v106
	v_cvt_f64_f32_e32 v[72:73], v116
	v_fmac_f64_e32 v[92:93], v[70:71], v[72:73]
	v_cvt_f64_f32_e32 v[70:71], v107
	v_cvt_f64_f32_e32 v[72:73], v117
	v_fmac_f64_e32 v[94:95], v[70:71], v[72:73]
	v_cvt_f64_f32_e32 v[70:71], v108
	v_cvt_f64_f32_e32 v[72:73], v118
	ds_read_b128 v[50:53], v250 offset:11520
	s_nop 0
	ds_read_b128 v[62:65], v250 offset:11264
	v_fmac_f64_e32 v[92:93], v[70:71], v[72:73]
	global_load_dwordx4 v[70:73], v[110:111], off offset:16
	global_load_dwordx4 v[120:123], v[110:111], off
	v_cvt_f64_f32_e32 v[106:107], v109
	v_cvt_f64_f32_e32 v[108:109], v119
	v_fmac_f64_e32 v[94:95], v[106:107], v[108:109]
	s_waitcnt lgkmcnt(14)
	v_cvt_f64_f32_e32 v[106:107], v128
	s_waitcnt vmcnt(14)
	v_cvt_f64_f32_e32 v[108:109], v136
	v_fmac_f64_e32 v[92:93], v[106:107], v[108:109]
	v_cvt_f64_f32_e32 v[106:107], v129
	v_cvt_f64_f32_e32 v[108:109], v137
	v_fmac_f64_e32 v[94:95], v[106:107], v[108:109]
	v_cvt_f64_f32_e32 v[106:107], v130
	v_cvt_f64_f32_e32 v[108:109], v138
	v_fmac_f64_e32 v[92:93], v[106:107], v[108:109]
	v_cvt_f64_f32_e32 v[106:107], v131
	v_cvt_f64_f32_e32 v[108:109], v139
	v_fmac_f64_e32 v[94:95], v[106:107], v[108:109]
	v_cvt_f64_f32_e32 v[106:107], v124
	v_cvt_f64_f32_e32 v[108:109], v132
	v_fmac_f64_e32 v[92:93], v[106:107], v[108:109]
	v_cvt_f64_f32_e32 v[106:107], v125
	v_cvt_f64_f32_e32 v[108:109], v133
	v_fmac_f64_e32 v[94:95], v[106:107], v[108:109]
	v_cvt_f64_f32_e32 v[106:107], v126
	v_cvt_f64_f32_e32 v[108:109], v134
	v_fmac_f64_e32 v[92:93], v[106:107], v[108:109]
	v_cvt_f64_f32_e32 v[106:107], v127
	v_cvt_f64_f32_e32 v[108:109], v135
	v_fmac_f64_e32 v[94:95], v[106:107], v[108:109]
	s_waitcnt lgkmcnt(12)
	v_cvt_f64_f32_e32 v[106:107], v144
	s_waitcnt vmcnt(12)
	v_cvt_f64_f32_e32 v[108:109], v152
	v_fmac_f64_e32 v[92:93], v[106:107], v[108:109]
	v_cvt_f64_f32_e32 v[106:107], v145
	v_cvt_f64_f32_e32 v[108:109], v153
	v_fmac_f64_e32 v[94:95], v[106:107], v[108:109]
	v_cvt_f64_f32_e32 v[106:107], v146
	v_cvt_f64_f32_e32 v[108:109], v154
	v_fmac_f64_e32 v[92:93], v[106:107], v[108:109]
	v_cvt_f64_f32_e32 v[106:107], v147
	v_cvt_f64_f32_e32 v[108:109], v155
	v_fmac_f64_e32 v[94:95], v[106:107], v[108:109]
	v_cvt_f64_f32_e32 v[106:107], v140
	v_cvt_f64_f32_e32 v[108:109], v148
	v_fmac_f64_e32 v[92:93], v[106:107], v[108:109]
	v_cvt_f64_f32_e32 v[106:107], v141
	v_cvt_f64_f32_e32 v[108:109], v149
	v_fmac_f64_e32 v[94:95], v[106:107], v[108:109]
	v_cvt_f64_f32_e32 v[106:107], v142
	v_cvt_f64_f32_e32 v[108:109], v150
	v_fmac_f64_e32 v[92:93], v[106:107], v[108:109]
	v_cvt_f64_f32_e32 v[106:107], v143
	v_cvt_f64_f32_e32 v[108:109], v151
	v_fmac_f64_e32 v[94:95], v[106:107], v[108:109]
	s_waitcnt lgkmcnt(10)
	v_cvt_f64_f32_e32 v[106:107], v160
	s_waitcnt vmcnt(10)
	v_cvt_f64_f32_e32 v[108:109], v168
	v_fmac_f64_e32 v[92:93], v[106:107], v[108:109]
	v_cvt_f64_f32_e32 v[106:107], v161
	v_cvt_f64_f32_e32 v[108:109], v169
	v_fmac_f64_e32 v[94:95], v[106:107], v[108:109]
	v_cvt_f64_f32_e32 v[106:107], v162
	v_cvt_f64_f32_e32 v[108:109], v170
	v_fmac_f64_e32 v[92:93], v[106:107], v[108:109]
	v_cvt_f64_f32_e32 v[106:107], v163
	v_cvt_f64_f32_e32 v[108:109], v171
	v_fmac_f64_e32 v[94:95], v[106:107], v[108:109]
	v_cvt_f64_f32_e32 v[106:107], v156
	v_cvt_f64_f32_e32 v[108:109], v164
	v_fmac_f64_e32 v[92:93], v[106:107], v[108:109]
	v_cvt_f64_f32_e32 v[106:107], v157
	v_cvt_f64_f32_e32 v[108:109], v165
	v_fmac_f64_e32 v[94:95], v[106:107], v[108:109]
	v_cvt_f64_f32_e32 v[106:107], v158
	v_cvt_f64_f32_e32 v[108:109], v166
	v_fmac_f64_e32 v[92:93], v[106:107], v[108:109]
	v_cvt_f64_f32_e32 v[106:107], v159
	v_cvt_f64_f32_e32 v[108:109], v167
	v_fmac_f64_e32 v[94:95], v[106:107], v[108:109]
	s_waitcnt lgkmcnt(8)
	v_cvt_f64_f32_e32 v[106:107], v176
	s_waitcnt vmcnt(8)
	v_cvt_f64_f32_e32 v[108:109], v184
	v_fmac_f64_e32 v[92:93], v[106:107], v[108:109]
	v_cvt_f64_f32_e32 v[106:107], v177
	v_cvt_f64_f32_e32 v[108:109], v185
	v_fmac_f64_e32 v[94:95], v[106:107], v[108:109]
	v_cvt_f64_f32_e32 v[106:107], v178
	v_cvt_f64_f32_e32 v[108:109], v186
	v_fmac_f64_e32 v[92:93], v[106:107], v[108:109]
	v_cvt_f64_f32_e32 v[106:107], v179
	v_cvt_f64_f32_e32 v[108:109], v187
	v_fmac_f64_e32 v[94:95], v[106:107], v[108:109]
	v_cvt_f64_f32_e32 v[106:107], v172
	v_cvt_f64_f32_e32 v[108:109], v180
	v_fmac_f64_e32 v[92:93], v[106:107], v[108:109]
	v_cvt_f64_f32_e32 v[106:107], v173
	v_cvt_f64_f32_e32 v[108:109], v181
	v_fmac_f64_e32 v[94:95], v[106:107], v[108:109]
	v_cvt_f64_f32_e32 v[106:107], v174
	v_cvt_f64_f32_e32 v[108:109], v182
	v_fmac_f64_e32 v[92:93], v[106:107], v[108:109]
	v_cvt_f64_f32_e32 v[106:107], v175
	v_cvt_f64_f32_e32 v[108:109], v183
	v_fmac_f64_e32 v[94:95], v[106:107], v[108:109]
	s_waitcnt lgkmcnt(6)
	v_cvt_f64_f32_e32 v[106:107], v192
	s_waitcnt vmcnt(6)
	v_cvt_f64_f32_e32 v[108:109], v200
	v_fmac_f64_e32 v[92:93], v[106:107], v[108:109]
	v_cvt_f64_f32_e32 v[106:107], v193
	v_cvt_f64_f32_e32 v[108:109], v201
	v_fmac_f64_e32 v[94:95], v[106:107], v[108:109]
	v_cvt_f64_f32_e32 v[106:107], v194
	v_cvt_f64_f32_e32 v[108:109], v202
	v_fmac_f64_e32 v[92:93], v[106:107], v[108:109]
	v_cvt_f64_f32_e32 v[106:107], v195
	v_cvt_f64_f32_e32 v[108:109], v203
	v_fmac_f64_e32 v[94:95], v[106:107], v[108:109]
	v_cvt_f64_f32_e32 v[106:107], v188
	v_cvt_f64_f32_e32 v[108:109], v196
	v_fmac_f64_e32 v[92:93], v[106:107], v[108:109]
	v_cvt_f64_f32_e32 v[106:107], v189
	v_cvt_f64_f32_e32 v[108:109], v197
	v_fmac_f64_e32 v[94:95], v[106:107], v[108:109]
	v_cvt_f64_f32_e32 v[106:107], v190
	v_cvt_f64_f32_e32 v[108:109], v198
	v_fmac_f64_e32 v[92:93], v[106:107], v[108:109]
	v_cvt_f64_f32_e32 v[106:107], v191
	v_cvt_f64_f32_e32 v[108:109], v199
	v_fmac_f64_e32 v[94:95], v[106:107], v[108:109]
	s_waitcnt lgkmcnt(4)
	v_cvt_f64_f32_e32 v[106:107], v204
	s_waitcnt vmcnt(4)
	v_cvt_f64_f32_e32 v[108:109], v208
	v_fmac_f64_e32 v[92:93], v[106:107], v[108:109]
	v_cvt_f64_f32_e32 v[106:107], v205
	v_cvt_f64_f32_e32 v[108:109], v209
	v_fmac_f64_e32 v[94:95], v[106:107], v[108:109]
	v_cvt_f64_f32_e32 v[106:107], v206
	v_cvt_f64_f32_e32 v[108:109], v210
	v_fmac_f64_e32 v[92:93], v[106:107], v[108:109]
	v_cvt_f64_f32_e32 v[106:107], v207
	v_cvt_f64_f32_e32 v[108:109], v211
	v_fmac_f64_e32 v[94:95], v[106:107], v[108:109]
	v_cvt_f64_f32_e32 v[106:107], v74
	v_cvt_f64_f32_e32 v[108:109], v82
	v_cvt_f64_f32_e32 v[74:75], v75
	v_cvt_f64_f32_e32 v[82:83], v83
	v_fmac_f64_e32 v[92:93], v[106:107], v[108:109]
	v_fmac_f64_e32 v[94:95], v[74:75], v[82:83]
	v_cvt_f64_f32_e32 v[74:75], v76
	v_cvt_f64_f32_e32 v[82:83], v84
	v_fmac_f64_e32 v[92:93], v[74:75], v[82:83]
	v_cvt_f64_f32_e32 v[74:75], v77
	v_cvt_f64_f32_e32 v[76:77], v85
	v_fmac_f64_e32 v[94:95], v[74:75], v[76:77]
	s_waitcnt lgkmcnt(2)
	v_cvt_f64_f32_e32 v[74:75], v66
	s_waitcnt vmcnt(2)
	v_cvt_f64_f32_e32 v[76:77], v78
	v_fmac_f64_e32 v[92:93], v[74:75], v[76:77]
	v_cvt_f64_f32_e32 v[66:67], v67
	v_cvt_f64_f32_e32 v[74:75], v79
	v_fmac_f64_e32 v[94:95], v[66:67], v[74:75]
	v_cvt_f64_f32_e32 v[66:67], v68
	v_cvt_f64_f32_e32 v[74:75], v80
	v_fmac_f64_e32 v[92:93], v[66:67], v[74:75]
	v_cvt_f64_f32_e32 v[66:67], v69
	v_cvt_f64_f32_e32 v[68:69], v81
	v_fmac_f64_e32 v[94:95], v[66:67], v[68:69]
	v_cvt_f64_f32_e32 v[66:67], v54
	v_cvt_f64_f32_e32 v[68:69], v58
	v_cvt_f64_f32_e32 v[54:55], v55
	v_cvt_f64_f32_e32 v[58:59], v59
	v_fmac_f64_e32 v[92:93], v[66:67], v[68:69]
	v_fmac_f64_e32 v[94:95], v[54:55], v[58:59]
	v_cvt_f64_f32_e32 v[54:55], v56
	v_cvt_f64_f32_e32 v[58:59], v60
	v_fmac_f64_e32 v[92:93], v[54:55], v[58:59]
	v_cvt_f64_f32_e32 v[54:55], v57
	v_cvt_f64_f32_e32 v[56:57], v61
	v_fmac_f64_e32 v[94:95], v[54:55], v[56:57]
	s_waitcnt lgkmcnt(0)
	v_cvt_f64_f32_e32 v[54:55], v62
	s_waitcnt vmcnt(0)
	v_cvt_f64_f32_e32 v[56:57], v120
	v_fmac_f64_e32 v[92:93], v[54:55], v[56:57]
	v_cvt_f64_f32_e32 v[54:55], v63
	v_cvt_f64_f32_e32 v[56:57], v121
	v_fmac_f64_e32 v[94:95], v[54:55], v[56:57]
	v_cvt_f64_f32_e32 v[54:55], v64
	v_cvt_f64_f32_e32 v[56:57], v122
	v_fmac_f64_e32 v[92:93], v[54:55], v[56:57]
	v_cvt_f64_f32_e32 v[54:55], v65
	v_cvt_f64_f32_e32 v[56:57], v123
	v_fmac_f64_e32 v[94:95], v[54:55], v[56:57]
	v_cvt_f64_f32_e32 v[54:55], v50
	v_cvt_f64_f32_e32 v[56:57], v70
	v_fmac_f64_e32 v[92:93], v[54:55], v[56:57]
	v_cvt_f64_f32_e32 v[50:51], v51
	v_cvt_f64_f32_e32 v[54:55], v71
	v_fmac_f64_e32 v[94:95], v[50:51], v[54:55]
	v_cvt_f64_f32_e32 v[50:51], v52
	v_cvt_f64_f32_e32 v[54:55], v72
	v_fmac_f64_e32 v[92:93], v[50:51], v[54:55]
	v_cvt_f64_f32_e32 v[50:51], v53
	v_cvt_f64_f32_e32 v[52:53], v73
	v_fmac_f64_e32 v[94:95], v[50:51], v[52:53]
	v_add_f64 v[50:51], v[92:93], v[94:95]
	s_nop 1
	v_mov_b32_dpp v52, v50 quad_perm:[1,0,3,2] row_mask:0xf bank_mask:0xf
	v_mov_b32_dpp v53, v51 quad_perm:[1,0,3,2] row_mask:0xf bank_mask:0xf
	s_waitcnt lgkmcnt(0)
	v_add_f64 v[50:51], v[50:51], v[52:53]
	s_nop 1
	v_mov_b32_dpp v52, v50 quad_perm:[2,3,0,1] row_mask:0xf bank_mask:0xf
	v_mov_b32_dpp v53, v51 quad_perm:[2,3,0,1] row_mask:0xf bank_mask:0xf
	s_waitcnt lgkmcnt(0)
	v_add_f64 v[50:51], v[50:51], v[52:53]
	s_nop 1
	v_mov_b32_dpp v52, v50 row_half_mirror row_mask:0xf bank_mask:0xf
	v_mov_b32_dpp v53, v51 row_half_mirror row_mask:0xf bank_mask:0xf
	s_waitcnt lgkmcnt(0)
	v_add_f64 v[50:51], v[50:51], v[52:53]
	s_nop 1
	v_mov_b32_dpp v52, v50 row_mirror row_mask:0xf bank_mask:0xf
	v_mov_b32_dpp v53, v51 row_mirror row_mask:0xf bank_mask:0xf
	s_and_saveexec_b64 s[0:1], vcc
	s_cbranch_execz .LBB2_168
	v_lshrrev_b32_e32 v0, 8, v105
	v_lshl_add_u32 v0, v0, 3, 0
	v_lshl_add_u32 v54, v104, 3, 0
	v_add_u32_e32 v0, 0x13450, v0
	v_add_u32_e32 v56, 0x12ed0, v54
	ds_read_b64 v[54:55], v0
	ds_read_b64 v[56:57], v56
	s_waitcnt lgkmcnt(2)
	v_add_f64 v[50:51], v[50:51], v[52:53]
	s_waitcnt lgkmcnt(1)
	v_mul_f64 v[50:51], v[50:51], v[54:55]
	s_waitcnt lgkmcnt(0)
	v_mul_f64 v[50:51], v[50:51], v[56:57]
	ds_write_b64 v101, v[50:51]
	s_branch .LBB2_168

	.amdhsa_kernel _Z7k_fine3PKfS0_PKtS2_PKdS4_S0_PiPfS5_S0_S0_PtS7_
		.amdhsa_group_segment_fixed_size 30768
		.amdhsa_private_segment_fixed_size 0
		.amdhsa_kernarg_size 112
		.amdhsa_user_sgpr_count 2
		.amdhsa_user_sgpr_dispatch_ptr 0
		.amdhsa_user_sgpr_queue_ptr 0
		.amdhsa_user_sgpr_kernarg_segment_ptr 1
		.amdhsa_user_sgpr_dispatch_id 0
		.amdhsa_user_sgpr_kernarg_preload_length 0
		.amdhsa_user_sgpr_kernarg_preload_offset 0
		.amdhsa_user_sgpr_private_segment_size 0
		.amdhsa_uses_dynamic_stack 0
		.amdhsa_enable_private_segment 0
		.amdhsa_system_sgpr_workgroup_id_x 1
		.amdhsa_system_sgpr_workgroup_id_y 0
		.amdhsa_system_sgpr_workgroup_id_z 0
		.amdhsa_system_sgpr_workgroup_info 0
		.amdhsa_system_vgpr_workitem_id 0
		.amdhsa_next_free_vgpr 256
		.amdhsa_next_free_sgpr 100
		.amdhsa_accum_offset 256
		.amdhsa_reserve_vcc 1
		.amdhsa_float_round_mode_32 0
		.amdhsa_float_round_mode_16_64 0
		.amdhsa_float_denorm_mode_32 3
		.amdhsa_float_denorm_mode_16_64 3
		.amdhsa_dx10_clamp 1
		.amdhsa_ieee_mode 1
		.amdhsa_fp16_overflow 0
		.amdhsa_tg_split 0
		.amdhsa_exception_fp_ieee_invalid_op 0
		.amdhsa_exception_fp_denorm_src 0
		.amdhsa_exception_fp_ieee_div_zero 0
		.amdhsa_exception_fp_ieee_overflow 0
		.amdhsa_exception_fp_ieee_underflow 0
		.amdhsa_exception_fp_ieee_inexact 0
		.amdhsa_exception_int_div_zero 0
	.end_amdhsa_kernel

amdhsa.kernels:
  - .agpr_count:     0
    .args:
      - .actual_access:  read_only
        .address_space:  global
        .offset:         0
        .size:           8
        .value_kind:     global_buffer
      - .actual_access:  read_only
        .address_space:  global
        .offset:         8
        .size:           8
        .value_kind:     global_buffer
      - .actual_access:  write_only
        .address_space:  global
        .offset:         16
        .size:           8
        .value_kind:     global_buffer
      - .actual_access:  write_only
        .address_space:  global
        .offset:         24
        .size:           8
        .value_kind:     global_buffer
      - .actual_access:  write_only
        .address_space:  global
        .offset:         32
        .size:           8
        .value_kind:     global_buffer
      - .actual_access:  write_only
        .address_space:  global
        .offset:         40
        .size:           8
        .value_kind:     global_buffer
      - .actual_access:  write_only
        .address_space:  global
        .offset:         48
        .size:           8
        .value_kind:     global_buffer
      - .actual_access:  write_only
        .address_space:  global
        .offset:         56
        .size:           8
        .value_kind:     global_buffer
      - .actual_access:  write_only
        .address_space:  global
        .offset:         64
        .size:           8
        .value_kind:     global_buffer
    .group_segment_fixed_size: 18944
    .kernarg_segment_align: 8
    .kernarg_segment_size: 72
    .language:       OpenCL C
    .language_version:
      - 2
      - 0
    .max_flat_workgroup_size: 256
    .name:           _Z6k_prepPKfS0_PfS1_PdS2_PtS3_S3_
    .private_segment_fixed_size: 0
    .sgpr_count:     34
    .sgpr_spill_count: 0
    .symbol:         _Z6k_prepPKfS0_PfS1_PdS2_PtS3_S3_.kd
    .uniform_work_group_size: 1
    .uses_dynamic_stack: false
    .vgpr_count:     29
    .vgpr_spill_count: 0
    .wavefront_size: 64
  - .agpr_count:     16
    .args:
      - .actual_access:  read_only
        .address_space:  global
        .offset:         0
        .size:           8
        .value_kind:     global_buffer
      - .actual_access:  read_only
        .address_space:  global
        .offset:         8
        .size:           8
        .value_kind:     global_buffer
      - .actual_access:  read_only
        .address_space:  global
        .offset:         16
        .size:           8
        .value_kind:     global_buffer
      - .actual_access:  read_only
        .address_space:  global
        .offset:         24
        .size:           8
        .value_kind:     global_buffer
      - .actual_access:  write_only
        .address_space:  global
        .offset:         32
        .size:           8
        .value_kind:     global_buffer
    .group_segment_fixed_size: 256
    .kernarg_segment_align: 8
    .kernarg_segment_size: 40
    .language:       OpenCL C
    .language_version:
      - 2
      - 0
    .max_flat_workgroup_size: 256
    .name:           _Z9k_coarse2PKtS0_PKdS2_Pf
    .private_segment_fixed_size: 0
    .sgpr_count:     37
    .sgpr_spill_count: 0
    .symbol:         _Z9k_coarse2PKtS0_PKdS2_Pf.kd
    .uniform_work_group_size: 1
    .uses_dynamic_stack: false
    .vgpr_count:     156
    .vgpr_spill_count: 0
    .wavefront_size: 64
  - .agpr_count:     0
    .args:
      - .actual_access:  read_only
        .address_space:  global
        .offset:         0
        .size:           8
        .value_kind:     global_buffer
      - .actual_access:  read_only
        .address_space:  global
        .offset:         8
        .size:           8
        .value_kind:     global_buffer
      - .actual_access:  read_only
        .address_space:  global
        .offset:         16
        .size:           8
        .value_kind:     global_buffer
      - .actual_access:  read_only
        .address_space:  global
        .offset:         24
        .size:           8
        .value_kind:     global_buffer
      - .actual_access:  read_only
        .address_space:  global
        .offset:         32
        .size:           8
        .value_kind:     global_buffer
      - .actual_access:  read_only
        .address_space:  global
        .offset:         40
        .size:           8
        .value_kind:     global_buffer
      - .actual_access:  read_only
        .address_space:  global
        .offset:         48
        .size:           8
        .value_kind:     global_buffer
      - .actual_access:  write_only
        .address_space:  global
        .offset:         56
        .size:           8
        .value_kind:     global_buffer
      - .actual_access:  write_only
        .address_space:  global
        .offset:         64
        .size:           8
        .value_kind:     global_buffer
      - .actual_access:  write_only
        .address_space:  global
        .offset:         72
        .size:           8
        .value_kind:     global_buffer
      - .actual_access:  read_only
        .address_space:  global
        .offset:         80
        .size:           8
        .value_kind:     global_buffer
      - .actual_access:  read_only
        .address_space:  global
        .offset:         88
        .size:           8
        .value_kind:     global_buffer
      - .actual_access:  write_only
        .address_space:  global
        .offset:         96
        .size:           8
        .value_kind:     global_buffer
      - .actual_access:  write_only
        .address_space:  global
        .offset:         104
        .size:           8
        .value_kind:     global_buffer
    .group_segment_fixed_size: 30768
    .kernarg_segment_align: 8
    .kernarg_segment_size: 112
    .language:       OpenCL C
    .language_version:
      - 2
      - 0
    .max_flat_workgroup_size: 512
    .name:           _Z7k_fine3PKfS0_PKtS2_PKdS4_S0_PiPfS5_S0_S0_PtS7_
    .private_segment_fixed_size: 0
    .sgpr_count:     106
    .sgpr_spill_count: 4
    .symbol:         _Z7k_fine3PKfS0_PKtS2_PKdS4_S0_PiPfS5_S0_S0_PtS7_.kd
    .uniform_work_group_size: 1
    .uses_dynamic_stack: false
    .vgpr_count:     256
    .vgpr_spill_count: 0
    .wavefront_size: 64
  - .agpr_count:     0
    .args:
      - .actual_access:  read_only
        .address_space:  global
        .offset:         0
        .size:           8
        .value_kind:     global_buffer
      - .actual_access:  read_only
        .address_space:  global
        .offset:         8
        .size:           8
        .value_kind:     global_buffer
      - .actual_access:  read_only
        .address_space:  global
        .offset:         16
        .size:           8
        .value_kind:     global_buffer
      - .actual_access:  read_only
        .address_space:  global
        .offset:         24
        .size:           8
        .value_kind:     global_buffer
      - .actual_access:  read_only
        .address_space:  global
        .offset:         32
        .size:           8
        .value_kind:     global_buffer
      - .actual_access:  read_only
        .address_space:  global
        .offset:         40
        .size:           8
        .value_kind:     global_buffer
      - .actual_access:  write_only
        .address_space:  global
        .offset:         48
        .size:           8
        .value_kind:     global_buffer
      - .actual_access:  write_only
        .address_space:  global
        .offset:         56
        .size:           8
        .value_kind:     global_buffer
      - .actual_access:  write_only
        .address_space:  global
        .offset:         64
        .size:           8
        .value_kind:     global_buffer
    .group_segment_fixed_size: 18512
    .kernarg_segment_align: 8
    .kernarg_segment_size: 72
    .language:       OpenCL C
    .language_version:
      - 2
      - 0
    .max_flat_workgroup_size: 256
    .name:           _Z10k_transferPKtS0_PKfPKiS2_S4_PfS5_S5_
    .private_segment_fixed_size: 0
    .sgpr_count:     34
    .sgpr_spill_count: 0
    .symbol:         _Z10k_transferPKtS0_PKfPKiS2_S4_PfS5_S5_.kd
    .uniform_work_group_size: 1
    .uses_dynamic_stack: false
    .vgpr_count:     49
    .vgpr_spill_count: 0
    .wavefront_size: 64
